# code placement, opposite phase: every GEMM MFMA encoding at byte phase 4 (pad s_nop in front of the preceding load segment's closing wait)
# speedup vs baseline: 1.0067x; 1.0067x over previous
; #define PG8_STAGE(bufoff, gbase, voff) do { _Pragma("unroll") for (int _i = 0; _i < 2; ++_i) \
;         __builtin_amdgcn_global_load_lds((const unsigned*)((const char*)(gbase) + (voff)[_i]), (LAS unsigned*)(lds + (bufoff) + ldsw + _i * 8192), 16, 0, 0); } while (0)
; #define PG8_LDA(dst, b, h) do { _Pragma("unroll") for (int m = 0; m < 4; ++m) dst[m] = PG8_LD32(lds + PG8_SA(b, h) + aoff + m * 2048); } while (0)
; #define PG8_LDB(dst, b, h) do { _Pragma("unroll") for (int n = 0; n < 2; ++n) dst[n] = PG8_LD32(lds + PG8_SB(b, h) + boff + n * 2048); } while (0)
; #define PG8_WAIT_V(n) asm volatile("s_waitcnt vmcnt(" #n ")" ::: "memory")
; #define PG8_WAIT_L(n) asm volatile("s_waitcnt lgkmcnt(" #n ")" ::: "memory")
; #define PG8_BAR __builtin_amdgcn_s_barrier()
; #define PG8_SCHED __builtin_amdgcn_sched_barrier(0)
; #define PG8_STA(bufoff, nextflag, h, koff) do { if constexpr (Sched::GATHER) { unsigned _o[2]; _o[0] = (nextflag) ? nxtA[h][0] : curA[h][0]; _o[1] = (nextflag) ? nxtA[h][1] : curA[h][1]; PG8_STAGE(bufoff, Ab + (koff), _o); } \
;         else { PG8_STAGE(bufoff, ((nextflag) ? nA : cA) + (size_t)(h) * hstep + (koff), voffA); } } while (0)
; template <class Epi, class Sched, bool ALIGN_EPI, int DT>
; __device__ __forceinline__ void gemm_phase(LAS unsigned char* lds, const int KB, const Sched& S, const Epi& E) {
;     ...
;             PG8_LDB(B0, 0, 0); PG8_LDB(B1, 0, 1); PG8_SCHED; PG8_LDA(At, 0, 0); PG8_STA(PG8_SA(1, 1), false, 1, k1);
;             PG8_WAIT_V(8); PG8_WAIT_L(0); PG8_BAR; PG8_MMA(0, 0, At, B0); PG8_MMA(0, 1, At, B1); PG8_BAR; PG8_SCHED;
;             PG8_LDA(At, 0, 1); PG8_STAGE(PG8_SB(0, 0), b2, voffB); PG8_STAGE(PG8_SB(0, 1), b2 + hstep, voffB); PG8_STA(PG8_SA(0, 0), last, 0, k2);
;             PG8_WAIT_V(8); PG8_WAIT_L(0); PG8_BAR; PG8_MMA(1, 0, At, B0); PG8_MMA(1, 1, At, B1); PG8_BAR; PG8_SCHED;
.LBB0_193:
	ds_read_b128 v[152:155], v175
	ds_read_b128 v[156:159], v175 offset:1024
	ds_read_b128 v[160:163], v175 offset:2048
	ds_read_b128 v[164:167], v175 offset:3072
	ds_read_b128 v[168:171], v176
	ds_read_b128 v[182:185], v176 offset:1024
	ds_read_b128 v[186:189], v176 offset:2048
	ds_read_b128 v[190:193], v176 offset:3072
	s_add_u32 s38, s36, 0x100
	s_addc_u32 s39, s37, 0
	s_add_u32 s68, s25, s36
	s_addc_u32 s69, s66, s37
	s_cmp_eq_u32 s67, 12
	s_cselect_b64 s[42:43], -1, 0
	s_and_b64 s[40:41], s[42:43], exec
	s_cselect_b32 s70, 0, s38
	s_cselect_b32 s41, s0, s69
	s_cselect_b32 s40, s23, s68
	v_lshl_add_u64 v[228:229], v[148:149], 0, s[36:37]
	s_add_i32 m0, s45, 0xc000
	ds_read_b128 v[196:199], v177
	ds_read_b128 v[200:203], v177 offset:1024
	ds_read_b128 v[204:207], v177 offset:2048
	ds_read_b128 v[208:211], v177 offset:3072
	ds_read_b128 v[212:215], v177 offset:4096
	ds_read_b128 v[216:219], v177 offset:5120
	ds_read_b128 v[220:223], v177 offset:6144
	ds_read_b128 v[224:227], v177 offset:7168
	global_load_lds_dwordx4 v[228:229], off
	v_lshl_add_u64 v[228:229], v[150:151], 0, s[36:37]
	s_add_i32 m0, s45, 0xe000
	s_nop 0
	global_load_lds_dwordx4 v[228:229], off
	s_nop 0
	s_waitcnt vmcnt(8)
	s_waitcnt lgkmcnt(0)
	s_barrier
	s_setprio 1
	s_waitcnt lgkmcnt(0)
	v_mfma_i32_16x16x64_i8 v[126:129], v[152:155], v[196:199], v[126:129]
	v_mfma_i32_16x16x64_i8 v[122:125], v[160:163], v[196:199], v[122:125]
	v_mfma_i32_16x16x64_i8 v[110:113], v[152:155], v[204:207], v[110:113]
	v_mfma_i32_16x16x64_i8 v[106:109], v[160:163], v[204:207], v[106:109]
	v_mfma_i32_16x16x64_i8 v[94:97], v[152:155], v[212:215], v[94:97]
	v_mfma_i32_16x16x64_i8 v[90:93], v[160:163], v[212:215], v[90:93]
	v_mfma_i32_16x16x64_i8 v[78:81], v[152:155], v[220:223], v[78:81]
	v_mfma_i32_16x16x64_i8 v[74:77], v[160:163], v[220:223], v[74:77]
	v_mfma_i32_16x16x64_i8 v[126:129], v[156:159], v[200:203], v[126:129]
	v_mfma_i32_16x16x64_i8 v[122:125], v[164:167], v[200:203], v[122:125]
	v_mfma_i32_16x16x64_i8 v[110:113], v[156:159], v[208:211], v[110:113]
	v_mfma_i32_16x16x64_i8 v[106:109], v[164:167], v[208:211], v[106:109]
	v_mfma_i32_16x16x64_i8 v[94:97], v[156:159], v[216:219], v[94:97]
	v_mfma_i32_16x16x64_i8 v[90:93], v[164:167], v[216:219], v[90:93]
	v_mfma_i32_16x16x64_i8 v[78:81], v[156:159], v[224:227], v[78:81]
	v_mfma_i32_16x16x64_i8 v[74:77], v[164:167], v[224:227], v[74:77]
	s_setprio 0
	s_setprio 1
	v_mfma_i32_16x16x64_i8 v[118:121], v[168:171], v[196:199], v[118:121]
	v_mfma_i32_16x16x64_i8 v[114:117], v[186:189], v[196:199], v[114:117]
	v_mfma_i32_16x16x64_i8 v[102:105], v[168:171], v[204:207], v[102:105]
	v_mfma_i32_16x16x64_i8 v[98:101], v[186:189], v[204:207], v[98:101]
	v_mfma_i32_16x16x64_i8 v[86:89], v[168:171], v[212:215], v[86:89]
	v_mfma_i32_16x16x64_i8 v[82:85], v[186:189], v[212:215], v[82:85]
	v_mfma_i32_16x16x64_i8 v[70:73], v[168:171], v[220:223], v[70:73]
	v_mfma_i32_16x16x64_i8 v[66:69], v[186:189], v[220:223], v[66:69]
	v_mfma_i32_16x16x64_i8 v[118:121], v[182:185], v[200:203], v[118:121]
	v_mfma_i32_16x16x64_i8 v[114:117], v[190:193], v[200:203], v[114:117]
	v_mfma_i32_16x16x64_i8 v[102:105], v[182:185], v[208:211], v[102:105]
	v_mfma_i32_16x16x64_i8 v[98:101], v[190:193], v[208:211], v[98:101]
	v_mfma_i32_16x16x64_i8 v[86:89], v[182:185], v[216:219], v[86:89]
	v_mfma_i32_16x16x64_i8 v[82:85], v[190:193], v[216:219], v[82:85]
	v_mfma_i32_16x16x64_i8 v[70:73], v[182:185], v[224:227], v[70:73]
	v_mfma_i32_16x16x64_i8 v[66:69], v[190:193], v[224:227], v[66:69]
	s_setprio 0
	s_barrier
	s_add_i32 s36, s62, s5
	v_lshl_add_u64 v[228:229], s[40:41], 0, v[134:135]
	s_mov_b32 m0, s36
	ds_read_b128 v[196:199], v177 offset:16384
	ds_read_b128 v[200:203], v177 offset:17408
	ds_read_b128 v[204:207], v177 offset:18432
	ds_read_b128 v[208:211], v177 offset:19456
	ds_read_b128 v[212:215], v177 offset:20480
	ds_read_b128 v[216:219], v177 offset:21504
	ds_read_b128 v[220:223], v177 offset:22528
	ds_read_b128 v[224:227], v177 offset:23552
	global_load_lds_dwordx4 v[228:229], off
	s_add_i32 m0, s36, 0x2000
	s_add_u32 s36, s40, 0x40000
	v_lshl_add_u64 v[230:231], s[40:41], 0, v[132:133]
	s_addc_u32 s37, s41, 0
	s_add_i32 s68, s63, s5
	global_load_lds_dwordx4 v[230:231], off
	v_lshl_add_u64 v[232:233], s[36:37], 0, v[134:135]
	s_mov_b32 m0, s68
	s_nop 0
	global_load_lds_dwordx4 v[232:233], off
	v_lshl_add_u64 v[232:233], s[36:37], 0, v[132:133]
	s_add_i32 m0, s68, 0x2000
	s_and_b64 s[36:37], s[8:9], s[42:43]
	s_and_b64 s[36:37], s[36:37], exec
	s_cselect_b32 s36, s26, s34
	s_cselect_b32 s37, s27, s35
	s_add_u32 s36, s36, s70
	s_addc_u32 s37, s37, 0
	global_load_lds_dwordx4 v[232:233], off
	v_lshl_add_u64 v[232:233], s[36:37], 0, v[136:137]
	s_mov_b32 m0, s45
	v_lshl_add_u64 v[234:235], s[36:37], 0, v[138:139]
	global_load_lds_dwordx4 v[232:233], off
	s_mov_b32 m0, s46
	s_nop 0
	global_load_lds_dwordx4 v[234:235], off
	s_waitcnt vmcnt(8)
	s_waitcnt lgkmcnt(0)
	s_barrier
; #define PG8_LDA(dst, b, h) do { _Pragma("unroll") for (int m = 0; m < 4; ++m) dst[m] = PG8_LD32(lds + PG8_SA(b, h) + aoff + m * 2048); } while (0)
; #define PG8_LDB(dst, b, h) do { _Pragma("unroll") for (int n = 0; n < 2; ++n) dst[n] = PG8_LD32(lds + PG8_SB(b, h) + boff + n * 2048); } while (0)
; #define PG8_WAIT_V(n) asm volatile("s_waitcnt vmcnt(" #n ")" ::: "memory")
; #define PG8_WAIT_L(n) asm volatile("s_waitcnt lgkmcnt(" #n ")" ::: "memory")
; #define PG8_BAR __builtin_amdgcn_s_barrier()
; #define PG8_SCHED __builtin_amdgcn_sched_barrier(0)
; #define PG8_STA(bufoff, nextflag, h, koff) do { if constexpr (Sched::GATHER) { unsigned _o[2]; _o[0] = (nextflag) ? nxtA[h][0] : curA[h][0]; _o[1] = (nextflag) ? nxtA[h][1] : curA[h][1]; PG8_STAGE(bufoff, Ab + (koff), _o); } \
;         else { PG8_STAGE(bufoff, ((nextflag) ? nA : cA) + (size_t)(h) * hstep + (koff), voffA); } } while (0)
; template <class Epi, class Sched, bool ALIGN_EPI, int DT>
; __device__ __forceinline__ void gemm_phase(LAS unsigned char* lds, const int KB, const Sched& S, const Epi& E) {
;     ...
;             PG8_WAIT_V(8); PG8_WAIT_L(0); PG8_BAR; PG8_MMA(1, 0, At, B0); PG8_MMA(1, 1, At, B1); PG8_BAR; PG8_SCHED;
;             PG8_LDB(B0, 1, 0); PG8_LDB(B1, 1, 1); PG8_SCHED; PG8_LDA(At, 1, 0); PG8_STA(PG8_SA(0, 1), last, 1, k2);
;             PG8_WAIT_V(8); PG8_WAIT_L(0); PG8_BAR; PG8_MMA(0, 0, At, B0); PG8_MMA(0, 1, At, B1); PG8_BAR; PG8_SCHED;
	s_setprio 1
	s_waitcnt lgkmcnt(0)
	v_mfma_i32_16x16x64_i8 v[62:65], v[152:155], v[196:199], v[62:65]
	v_mfma_i32_16x16x64_i8 v[58:61], v[160:163], v[196:199], v[58:61]
	v_mfma_i32_16x16x64_i8 v[46:49], v[152:155], v[204:207], v[46:49]
	v_mfma_i32_16x16x64_i8 v[42:45], v[160:163], v[204:207], v[42:45]
	v_mfma_i32_16x16x64_i8 v[30:33], v[152:155], v[212:215], v[30:33]
	v_mfma_i32_16x16x64_i8 v[26:29], v[160:163], v[212:215], v[26:29]
	v_mfma_i32_16x16x64_i8 v[6:9], v[152:155], v[220:223], v[6:9]
	v_mfma_i32_16x16x64_i8 v[2:5], v[160:163], v[220:223], v[2:5]
	v_mfma_i32_16x16x64_i8 v[62:65], v[156:159], v[200:203], v[62:65]
	v_mfma_i32_16x16x64_i8 v[58:61], v[164:167], v[200:203], v[58:61]
	v_mfma_i32_16x16x64_i8 v[46:49], v[156:159], v[208:211], v[46:49]
	v_mfma_i32_16x16x64_i8 v[42:45], v[164:167], v[208:211], v[42:45]
	v_mfma_i32_16x16x64_i8 v[30:33], v[156:159], v[216:219], v[30:33]
	v_mfma_i32_16x16x64_i8 v[26:29], v[164:167], v[216:219], v[26:29]
	v_mfma_i32_16x16x64_i8 v[6:9], v[156:159], v[224:227], v[6:9]
	v_mfma_i32_16x16x64_i8 v[2:5], v[164:167], v[224:227], v[2:5]
	s_setprio 0
	s_setprio 1
	v_mfma_i32_16x16x64_i8 v[54:57], v[168:171], v[196:199], v[54:57]
	v_mfma_i32_16x16x64_i8 v[50:53], v[186:189], v[196:199], v[50:53]
	v_mfma_i32_16x16x64_i8 v[38:41], v[168:171], v[204:207], v[38:41]
	v_mfma_i32_16x16x64_i8 v[34:37], v[186:189], v[204:207], v[34:37]
	v_mfma_i32_16x16x64_i8 v[14:17], v[168:171], v[212:215], v[14:17]
	v_mfma_i32_16x16x64_i8 v[10:13], v[186:189], v[212:215], v[10:13]
	v_mfma_i32_16x16x64_i8 v[22:25], v[168:171], v[220:223], v[22:25]
	v_mfma_i32_16x16x64_i8 v[18:21], v[186:189], v[220:223], v[18:21]
	v_mfma_i32_16x16x64_i8 v[54:57], v[182:185], v[200:203], v[54:57]
	v_mfma_i32_16x16x64_i8 v[50:53], v[190:193], v[200:203], v[50:53]
	v_mfma_i32_16x16x64_i8 v[38:41], v[182:185], v[208:211], v[38:41]
	v_mfma_i32_16x16x64_i8 v[34:37], v[190:193], v[208:211], v[34:37]
	v_mfma_i32_16x16x64_i8 v[14:17], v[182:185], v[216:219], v[14:17]
	v_mfma_i32_16x16x64_i8 v[10:13], v[190:193], v[216:219], v[10:13]
	v_mfma_i32_16x16x64_i8 v[22:25], v[182:185], v[224:227], v[22:25]
	v_mfma_i32_16x16x64_i8 v[18:21], v[190:193], v[224:227], v[18:21]
	s_setprio 0
	s_barrier
	s_add_i32 s42, 0, 0x18000
	v_add_u32_e32 v1, s42, v173
	s_add_i32 s43, 0, 0x1c000
	ds_read_b128 v[152:155], v1
	ds_read_b128 v[156:159], v1 offset:1024
	ds_read_b128 v[160:163], v1 offset:2048
	ds_read_b128 v[164:167], v1 offset:3072
	v_add_u32_e32 v1, s43, v173
	ds_read_b128 v[168:171], v1
	ds_read_b128 v[182:185], v1 offset:1024
	ds_read_b128 v[186:189], v1 offset:2048
	ds_read_b128 v[190:193], v1 offset:3072
	s_add_u32 s36, s36, 0x40000
	s_addc_u32 s37, s37, 0
	s_mov_b32 m0, s47
	v_lshl_add_u64 v[236:237], s[36:37], 0, v[136:137]
	ds_read_b128 v[196:199], v177 offset:32768
	ds_read_b128 v[200:203], v177 offset:33792
	ds_read_b128 v[204:207], v177 offset:34816
	ds_read_b128 v[208:211], v177 offset:35840
	ds_read_b128 v[212:215], v177 offset:36864
	ds_read_b128 v[216:219], v177 offset:37888
	ds_read_b128 v[220:223], v177 offset:38912
	ds_read_b128 v[224:227], v177 offset:39936
	global_load_lds_dwordx4 v[236:237], off
	v_lshl_add_u64 v[236:237], s[36:37], 0, v[138:139]
	s_mov_b32 m0, s49
	s_nop 0
	global_load_lds_dwordx4 v[236:237], off
	s_nop 0
	s_waitcnt vmcnt(8)
	s_waitcnt lgkmcnt(0)
	s_barrier
	s_setprio 1
	s_waitcnt lgkmcnt(0)
	v_mfma_i32_16x16x64_i8 v[126:129], v[152:155], v[196:199], v[126:129]
	v_mfma_i32_16x16x64_i8 v[122:125], v[160:163], v[196:199], v[122:125]
	v_mfma_i32_16x16x64_i8 v[110:113], v[152:155], v[204:207], v[110:113]
	v_mfma_i32_16x16x64_i8 v[106:109], v[160:163], v[204:207], v[106:109]
	v_mfma_i32_16x16x64_i8 v[94:97], v[152:155], v[212:215], v[94:97]
	v_mfma_i32_16x16x64_i8 v[90:93], v[160:163], v[212:215], v[90:93]
	v_mfma_i32_16x16x64_i8 v[78:81], v[152:155], v[220:223], v[78:81]
	v_mfma_i32_16x16x64_i8 v[74:77], v[160:163], v[220:223], v[74:77]
	v_mfma_i32_16x16x64_i8 v[126:129], v[156:159], v[200:203], v[126:129]
	v_mfma_i32_16x16x64_i8 v[122:125], v[164:167], v[200:203], v[122:125]
	v_mfma_i32_16x16x64_i8 v[110:113], v[156:159], v[208:211], v[110:113]
	v_mfma_i32_16x16x64_i8 v[106:109], v[164:167], v[208:211], v[106:109]
	v_mfma_i32_16x16x64_i8 v[94:97], v[156:159], v[216:219], v[94:97]
	v_mfma_i32_16x16x64_i8 v[90:93], v[164:167], v[216:219], v[90:93]
	v_mfma_i32_16x16x64_i8 v[78:81], v[156:159], v[224:227], v[78:81]
	v_mfma_i32_16x16x64_i8 v[74:77], v[164:167], v[224:227], v[74:77]
	s_setprio 0
	s_setprio 1
	v_mfma_i32_16x16x64_i8 v[118:121], v[168:171], v[196:199], v[118:121]
	v_mfma_i32_16x16x64_i8 v[114:117], v[186:189], v[196:199], v[114:117]
	v_mfma_i32_16x16x64_i8 v[102:105], v[168:171], v[204:207], v[102:105]
	v_mfma_i32_16x16x64_i8 v[98:101], v[186:189], v[204:207], v[98:101]
	v_mfma_i32_16x16x64_i8 v[86:89], v[168:171], v[212:215], v[86:89]
	v_mfma_i32_16x16x64_i8 v[82:85], v[186:189], v[212:215], v[82:85]
	v_mfma_i32_16x16x64_i8 v[70:73], v[168:171], v[220:223], v[70:73]
	v_mfma_i32_16x16x64_i8 v[66:69], v[186:189], v[220:223], v[66:69]
	v_mfma_i32_16x16x64_i8 v[118:121], v[182:185], v[200:203], v[118:121]
	v_mfma_i32_16x16x64_i8 v[114:117], v[190:193], v[200:203], v[114:117]
	v_mfma_i32_16x16x64_i8 v[102:105], v[182:185], v[208:211], v[102:105]
	v_mfma_i32_16x16x64_i8 v[98:101], v[190:193], v[208:211], v[98:101]
	v_mfma_i32_16x16x64_i8 v[86:89], v[182:185], v[216:219], v[86:89]
	v_mfma_i32_16x16x64_i8 v[82:85], v[190:193], v[216:219], v[82:85]
	v_mfma_i32_16x16x64_i8 v[70:73], v[182:185], v[224:227], v[70:73]
	v_mfma_i32_16x16x64_i8 v[66:69], v[190:193], v[224:227], v[66:69]
	s_setprio 0
	s_barrier
; #define PG8_STAGE(bufoff, gbase, voff) do { _Pragma("unroll") for (int _i = 0; _i < 2; ++_i) \
;         __builtin_amdgcn_global_load_lds((const unsigned*)((const char*)(gbase) + (voff)[_i]), (LAS unsigned*)(lds + (bufoff) + ldsw + _i * 8192), 16, 0, 0); } while (0)
; #define PG8_LDA(dst, b, h) do { _Pragma("unroll") for (int m = 0; m < 4; ++m) dst[m] = PG8_LD32(lds + PG8_SA(b, h) + aoff + m * 2048); } while (0)
; #define PG8_WAIT_V(n) asm volatile("s_waitcnt vmcnt(" #n ")" ::: "memory")
; #define PG8_WAIT_L(n) asm volatile("s_waitcnt lgkmcnt(" #n ")" ::: "memory")
; #define PG8_BAR __builtin_amdgcn_s_barrier()
; #define PG8_SCHED __builtin_amdgcn_sched_barrier(0)
; #define PG8_STA(bufoff, nextflag, h, koff) do { if constexpr (Sched::GATHER) { unsigned _o[2]; _o[0] = (nextflag) ? nxtA[h][0] : curA[h][0]; _o[1] = (nextflag) ? nxtA[h][1] : curA[h][1]; PG8_STAGE(bufoff, Ab + (koff), _o); } \
;         else { PG8_STAGE(bufoff, ((nextflag) ? nA : cA) + (size_t)(h) * hstep + (koff), voffA); } } while (0)
; template <class Epi, class Sched, bool ALIGN_EPI, int DT>
; __device__ __forceinline__ void gemm_phase(LAS unsigned char* lds, const int KB, const Sched& S, const Epi& E) {
;     ...
;             PG8_LDA(At, 1, 1); PG8_STAGE(PG8_SB(1, 0), b3, voffB); PG8_STAGE(PG8_SB(1, 1), b3 + hstep, voffB); PG8_STA(PG8_SA(1, 0), last, 0, k3);
;             PG8_WAIT_V(8); PG8_WAIT_L(0); PG8_BAR; PG8_MMA(1, 0, At, B0); PG8_MMA(1, 1, At, B1); PG8_BAR; PG8_SCHED;
;         }
;         if constexpr (ALIGN_EPI) { if (wr == 0) PG8_BAR; }
	s_add_i32 s36, s42, s5
	v_lshl_add_u64 v[228:229], v[228:229], 0, s[18:19]
	s_mov_b32 m0, s36
	ds_read_b128 v[196:199], v177 offset:49152
	ds_read_b128 v[200:203], v177 offset:50176
	ds_read_b128 v[204:207], v177 offset:51200
	ds_read_b128 v[208:211], v177 offset:52224
	ds_read_b128 v[212:215], v177 offset:53248
	ds_read_b128 v[216:219], v177 offset:54272
	ds_read_b128 v[220:223], v177 offset:55296
	ds_read_b128 v[224:227], v177 offset:56320
	global_load_lds_dwordx4 v[228:229], off
	s_add_i32 m0, s36, 0x2000
	s_add_u32 s36, s40, 0x40080
	v_lshl_add_u64 v[228:229], v[230:231], 0, s[18:19]
	s_addc_u32 s37, s41, 0
	s_add_i32 s40, s43, s5
	global_load_lds_dwordx4 v[228:229], off
	v_lshl_add_u64 v[228:229], s[36:37], 0, v[134:135]
	s_mov_b32 m0, s40
	s_nop 0
	global_load_lds_dwordx4 v[228:229], off
	v_lshl_add_u64 v[228:229], s[36:37], 0, v[132:133]
	s_add_i32 m0, s40, 0x2000
	s_nop 0
	global_load_lds_dwordx4 v[228:229], off
	v_lshl_add_u64 v[228:229], v[232:233], 0, s[18:19]
	s_mov_b32 m0, s55
	s_nop 0
	global_load_lds_dwordx4 v[228:229], off
	v_lshl_add_u64 v[228:229], v[234:235], 0, s[18:19]
	s_mov_b32 m0, s56
	s_nop 0
	global_load_lds_dwordx4 v[228:229], off
	s_waitcnt vmcnt(8)
	s_waitcnt lgkmcnt(0)
	s_barrier
	s_setprio 1
	s_waitcnt lgkmcnt(0)
	v_mfma_i32_16x16x64_i8 v[62:65], v[152:155], v[196:199], v[62:65]
	v_mfma_i32_16x16x64_i8 v[58:61], v[160:163], v[196:199], v[58:61]
	v_mfma_i32_16x16x64_i8 v[46:49], v[152:155], v[204:207], v[46:49]
	v_mfma_i32_16x16x64_i8 v[42:45], v[160:163], v[204:207], v[42:45]
	v_mfma_i32_16x16x64_i8 v[30:33], v[152:155], v[212:215], v[30:33]
	v_mfma_i32_16x16x64_i8 v[26:29], v[160:163], v[212:215], v[26:29]
	v_mfma_i32_16x16x64_i8 v[6:9], v[152:155], v[220:223], v[6:9]
	v_mfma_i32_16x16x64_i8 v[2:5], v[160:163], v[220:223], v[2:5]
	v_mfma_i32_16x16x64_i8 v[62:65], v[156:159], v[200:203], v[62:65]
	v_mfma_i32_16x16x64_i8 v[58:61], v[164:167], v[200:203], v[58:61]
	v_mfma_i32_16x16x64_i8 v[46:49], v[156:159], v[208:211], v[46:49]
	v_mfma_i32_16x16x64_i8 v[42:45], v[164:167], v[208:211], v[42:45]
	v_mfma_i32_16x16x64_i8 v[30:33], v[156:159], v[216:219], v[30:33]
	v_mfma_i32_16x16x64_i8 v[26:29], v[164:167], v[216:219], v[26:29]
	v_mfma_i32_16x16x64_i8 v[6:9], v[156:159], v[224:227], v[6:9]
	v_mfma_i32_16x16x64_i8 v[2:5], v[164:167], v[224:227], v[2:5]
	s_setprio 0
	s_setprio 1
	v_mfma_i32_16x16x64_i8 v[54:57], v[168:171], v[196:199], v[54:57]
	v_mfma_i32_16x16x64_i8 v[50:53], v[186:189], v[196:199], v[50:53]
	v_mfma_i32_16x16x64_i8 v[38:41], v[168:171], v[204:207], v[38:41]
	v_mfma_i32_16x16x64_i8 v[34:37], v[186:189], v[204:207], v[34:37]
	v_mfma_i32_16x16x64_i8 v[14:17], v[168:171], v[212:215], v[14:17]
	v_mfma_i32_16x16x64_i8 v[10:13], v[186:189], v[212:215], v[10:13]
	v_mfma_i32_16x16x64_i8 v[22:25], v[168:171], v[220:223], v[22:25]
	v_mfma_i32_16x16x64_i8 v[18:21], v[186:189], v[220:223], v[18:21]
	v_mfma_i32_16x16x64_i8 v[54:57], v[182:185], v[200:203], v[54:57]
	v_mfma_i32_16x16x64_i8 v[50:53], v[190:193], v[200:203], v[50:53]
	v_mfma_i32_16x16x64_i8 v[38:41], v[182:185], v[208:211], v[38:41]
	v_mfma_i32_16x16x64_i8 v[34:37], v[190:193], v[208:211], v[34:37]
	v_mfma_i32_16x16x64_i8 v[14:17], v[182:185], v[216:219], v[14:17]
	v_mfma_i32_16x16x64_i8 v[10:13], v[190:193], v[216:219], v[10:13]
	v_mfma_i32_16x16x64_i8 v[22:25], v[182:185], v[224:227], v[22:25]
	v_mfma_i32_16x16x64_i8 v[18:21], v[190:193], v[224:227], v[18:21]
	s_setprio 0
	s_barrier
	s_add_i32 s67, s67, 2
	s_cmp_gt_u32 s67, 13
	s_mov_b64 s[36:37], s[38:39]
	s_cbranch_scc0 .LBB0_193
	s_and_b64 vcc, exec, s[20:21]
	s_cbranch_vccz .LBB0_196
	s_barrier
